# w_e1 conversion loop: flat->global loads, counted vmcnt(16) per tile so four tiles stay in flight
# speedup vs baseline: 1.0062x; 1.0062x over previous
; #define LAS __attribute__((address_space(3)))
; #define TB_LOAD(R_, t_) do { const int _t = (t_); if (_t < tot) { const int _b = _t / per, _r = _t % per; ttb_load(R_, src + (size_t)_b * K_ * N_, N_, (_r % kt) * 128, (_r / kt) * 64, C.tid); } } while (0)
; __device__ __forceinline__ void ttb_load(TReg& R, const float* src, int ld, int k0, int n0, int tid) {
;     const int kr = tid >> 4, nq = tid & 15;
; #pragma unroll
;     for (int rep = 0; rep < 4; ++rep) R.v[rep] = __builtin_nontemporal_load((const f32x4*)(src + (size_t)(k0 + 4 * kr + rep) * ld + n0 + 4 * nq)); }
; __device__ __forceinline__ void ttb_put(const TReg& R, LAS unsigned* tile, int tid) {
;     const int kr = tid >> 4, nq = tid & 15;
; #pragma unroll
;     for (int c = 0; c < 4; ++c) { const int n = 4 * nq + c;
;         tile[n * 32 + (kr ^ (n & 31))] = pk4_fp8(R.v[0][c] * W_FP8_SCALE, R.v[1][c] * W_FP8_SCALE, R.v[2][c] * W_FP8_SCALE, R.v[3][c] * W_FP8_SCALE); } }
; __device__ __forceinline__ void ttb_finish(LAS const unsigned* tile, unsigned char* dst, int ldd, int k0, int n0, int map, int tid) {
;     const int n = tid >> 3, kq = tid & 7, m = n & 31, ns = n0 + n; int r = ns;
;     if (map == 2) { const int j = ns >> 1, par = ns & 1; r = 256 * (j >> 7) + 128 * par + (j & 127); }
;     const u32x4 g = *(LAS const u32x4*)(tile + n * 32 + 4 * (kq ^ (m >> 2)));
;     const unsigned a0 = (m & 1) ? g.y : g.x, a1 = (m & 1) ? g.x : g.y, a2 = (m & 1) ? g.w : g.z, a3 = (m & 1) ? g.z : g.w;
;     u32x4 w; w.x = (m & 2) ? a2 : a0; w.y = (m & 2) ? a3 : a1; w.z = (m & 2) ? a0 : a2; w.w = (m & 2) ? a1 : a3;
;     __builtin_nontemporal_store(w, (u32x4*)(dst + (size_t)r * ldd + k0 + 16 * kq));
; }
; template <int K_, int N_, int MAP_> __device__ __forceinline__ void tjob_b(const Ctx& C, int bid, int G, const float* src, unsigned char* dstb, int nbatch) {
;     constexpr int kt = K_ / 128, ntile = N_ / 64, per = kt * ntile; const int tot = per * nbatch;
;     TReg R0, R1, R2, R3; int kbuf = 0;
;     ...
;     TB_LOAD(R0, bid); TB_LOAD(R1, bid + G); TB_LOAD(R2, bid + 2 * G); TB_LOAD(R3, bid + 3 * G);
.LBB0_175:
	s_cmp_lt_i32 s72, 2
	s_cselect_b64 s[0:1], -1, 0
	s_cmp_gt_i32 s73, 1
	s_cselect_b64 s[2:3], -1, 0
	v_writelane_b32 v254, s60, 8
	s_and_b64 s[0:1], s[0:1], s[2:3]
	v_mov_b32_e32 v68, v0
	v_writelane_b32 v254, s61, 9
	v_cndmask_b32_e64 v1, 0, 1, s[0:1]
	v_writelane_b32 v254, s62, 10
	v_cmp_ne_u32_e64 s[4:5], 1, v1
	s_andn2_b64 vcc, exec, s[0:1]
	s_mov_b64 s[70:71], s[34:35]
	v_writelane_b32 v254, s63, 11
	s_cbranch_vccnz .LBB0_297
	v_readlane_b32 s0, v254, 2
	s_mov_b32 s6, s0
	s_and_b32 s0, s0, 7
	v_readlane_b32 s1, v254, 3
	s_cmp_eq_u32 s0, 0
	s_cselect_b64 s[0:1], -1, 0
	s_cmp_gt_i32 s6, 63
	s_cselect_b64 s[2:3], -1, 0
	s_mul_i32 s29, s6, 6
	s_and_b64 s[0:1], s[2:3], s[0:1]
	s_lshr_b32 s2, s29, 4
	s_and_b32 s2, s2, 0x7fffff8
	s_and_b64 s[0:1], s[0:1], exec
	s_cselect_b32 s30, s2, 0
	s_sub_i32 s28, s6, s30
	s_cmp_eq_u32 s30, 0
	s_cselect_b64 s[2:3], -1, 0
	s_cmp_lg_u32 s30, 0
	v_readlane_b32 s0, v254, 0
	s_cselect_b64 s[20:21], -1, 0
	s_cmp_lt_i32 s0, s28
	v_readlane_b32 s1, v254, 1
	s_cselect_b64 s[10:11], -1, 0
	s_and_b64 s[0:1], s[20:21], s[10:11]
	s_and_b64 vcc, exec, s[0:1]
	s_cbranch_vccnz .LBB0_228
	v_mov_b64_e32 v[2:3], s[70:71]
	flat_load_dwordx2 v[66:67], v[2:3] offset:184
	s_and_b64 s[0:1], s[2:3], exec
	s_cselect_b32 s0, 0, s28
	v_readlane_b32 s6, v254, 0
	s_sub_i32 s1, s6, s0
	v_readlane_b32 s7, v254, 1
	s_cmp_lt_i32 s1, 0x8000
	s_cselect_b64 s[6:7], -1, 0
	s_cmpk_gt_i32 s1, 0x7fff
	v_ashrrev_i32_e32 v69, 2, v68
	v_lshlrev_b32_e32 v74, 4, v68
	s_cbranch_scc1 .LBB0_179
	s_ashr_i32 s0, s1, 31
	s_lshr_b32 s0, s0, 22
	s_add_i32 s0, s1, s0
	s_ashr_i32 s8, s0, 10
	s_and_b32 s0, s0, 0xfc00
	s_sub_i32 s0, s1, s0
	s_sext_i32_i16 s12, s0
	s_bfe_u32 s12, s12, 0x4001b
	s_add_i32 s12, s0, s12
	s_sext_i32_i16 s13, s12
	s_and_b32 s12, s12, 0xfff0
	s_ashr_i32 s9, s8, 31
	s_sub_i32 s0, s0, s12
	s_lshl_b32 s12, s13, 2
	s_lshl_b64 s[8:9], s[8:9], 25
	s_sext_i32_i16 s0, s0
	s_andn2_b32 s12, s12, 63
	v_and_b32_e32 v1, -4, v69
	s_ashr_i32 s13, s12, 31
	s_waitcnt vmcnt(0) lgkmcnt(0)
	v_lshl_add_u64 v[2:3], v[66:67], 0, s[8:9]
	v_lshl_add_u32 v10, s0, 7, v1
	v_lshl_add_u64 v[2:3], s[12:13], 2, v[2:3]
	v_and_b32_e32 v4, 0xf0, v74
	v_mov_b32_e32 v5, 0
	v_ashrrev_i32_e32 v11, 31, v10
	v_lshl_add_u64 v[12:13], v[2:3], 0, v[4:5]
	v_lshlrev_b64 v[2:3], 14, v[10:11]
	v_lshl_add_u64 v[14:15], v[12:13], 0, v[2:3]
	v_or_b32_e32 v2, 1, v10
	v_ashrrev_i32_e32 v3, 31, v2
	v_lshlrev_b64 v[2:3], 14, v[2:3]
	v_lshl_add_u64 v[16:17], v[12:13], 0, v[2:3]
	global_load_dwordx4 v[2:5], v[14:15], off nt
	global_load_dwordx4 v[6:9], v[16:17], off nt
	v_or_b32_e32 v14, 2, v10
	v_ashrrev_i32_e32 v15, 31, v14
	v_or_b32_e32 v10, 3, v10
	v_lshlrev_b64 v[14:15], 14, v[14:15]
	v_ashrrev_i32_e32 v11, 31, v10
	v_lshl_add_u64 v[18:19], v[12:13], 0, v[14:15]
	v_lshlrev_b64 v[10:11], 14, v[10:11]
	v_lshl_add_u64 v[20:21], v[12:13], 0, v[10:11]
	global_load_dwordx4 v[10:13], v[18:19], off nt
	global_load_dwordx4 v[14:17], v[20:21], off nt
.LBB0_179:
	s_and_b64 s[8:9], s[2:3], exec
	v_readlane_b32 s8, v254, 2
	s_cselect_b32 s0, s8, s30
	s_add_i32 s22, s1, s0
	s_cmpk_gt_i32 s22, 0x7fff
	v_readlane_b32 s9, v254, 3
	s_cbranch_scc1 .LBB0_181
	s_ashr_i32 s8, s22, 31
	s_lshr_b32 s8, s8, 22
	s_add_i32 s9, s22, s8
	s_ashr_i32 s8, s9, 10
	s_and_b32 s9, s9, 0xfc00
	s_sub_i32 s12, s22, s9
	s_sext_i32_i16 s13, s12
	s_bfe_u32 s13, s13, 0x4001b
	s_add_i32 s13, s12, s13
	s_sext_i32_i16 s14, s13
	s_and_b32 s13, s13, 0xfff0
	s_sub_i32 s12, s12, s13
	s_ashr_i32 s9, s8, 31
	s_sext_i32_i16 s15, s12
	s_lshl_b32 s12, s14, 2
	s_lshl_b64 s[8:9], s[8:9], 25
	s_andn2_b32 s12, s12, 63
	v_and_b32_e32 v1, -4, v69
	s_ashr_i32 s13, s12, 31
	s_waitcnt vmcnt(0) lgkmcnt(0)
	v_lshl_add_u64 v[18:19], v[66:67], 0, s[8:9]
	v_lshl_add_u32 v26, s15, 7, v1
	v_lshl_add_u64 v[18:19], s[12:13], 2, v[18:19]
	v_and_b32_e32 v20, 0xf0, v74
	v_mov_b32_e32 v21, 0
	v_ashrrev_i32_e32 v27, 31, v26
	v_lshl_add_u64 v[28:29], v[18:19], 0, v[20:21]
	v_lshlrev_b64 v[18:19], 14, v[26:27]
	v_lshl_add_u64 v[30:31], v[28:29], 0, v[18:19]
	v_or_b32_e32 v18, 1, v26
	v_ashrrev_i32_e32 v19, 31, v18
	v_lshlrev_b64 v[18:19], 14, v[18:19]
	v_lshl_add_u64 v[32:33], v[28:29], 0, v[18:19]
	global_load_dwordx4 v[18:21], v[30:31], off nt
	global_load_dwordx4 v[22:25], v[32:33], off nt
	v_or_b32_e32 v30, 2, v26
	v_ashrrev_i32_e32 v31, 31, v30
	v_or_b32_e32 v26, 3, v26
	v_lshlrev_b64 v[30:31], 14, v[30:31]
	v_ashrrev_i32_e32 v27, 31, v26
	v_lshl_add_u64 v[34:35], v[28:29], 0, v[30:31]
	v_lshlrev_b64 v[26:27], 14, v[26:27]
	v_lshl_add_u64 v[36:37], v[28:29], 0, v[26:27]
	global_load_dwordx4 v[26:29], v[34:35], off nt
	global_load_dwordx4 v[30:33], v[36:37], off nt
; #define LAS __attribute__((address_space(3)))
; #define TB_LOAD(R_, t_) do { const int _t = (t_); if (_t < tot) { const int _b = _t / per, _r = _t % per; ttb_load(R_, src + (size_t)_b * K_ * N_, N_, (_r % kt) * 128, (_r / kt) * 64, C.tid); } } while (0)
; __device__ __forceinline__ void ttb_load(TReg& R, const float* src, int ld, int k0, int n0, int tid) {
;     const int kr = tid >> 4, nq = tid & 15;
; #pragma unroll
;     for (int rep = 0; rep < 4; ++rep) R.v[rep] = __builtin_nontemporal_load((const f32x4*)(src + (size_t)(k0 + 4 * kr + rep) * ld + n0 + 4 * nq)); }
; __device__ __forceinline__ void ttb_put(const TReg& R, LAS unsigned* tile, int tid) {
;     const int kr = tid >> 4, nq = tid & 15;
; #pragma unroll
;     for (int c = 0; c < 4; ++c) { const int n = 4 * nq + c;
;         tile[n * 32 + (kr ^ (n & 31))] = pk4_fp8(R.v[0][c] * W_FP8_SCALE, R.v[1][c] * W_FP8_SCALE, R.v[2][c] * W_FP8_SCALE, R.v[3][c] * W_FP8_SCALE); } }
; __device__ __forceinline__ void ttb_finish(LAS const unsigned* tile, unsigned char* dst, int ldd, int k0, int n0, int map, int tid) {
;     const int n = tid >> 3, kq = tid & 7, m = n & 31, ns = n0 + n; int r = ns;
;     if (map == 2) { const int j = ns >> 1, par = ns & 1; r = 256 * (j >> 7) + 128 * par + (j & 127); }
;     const u32x4 g = *(LAS const u32x4*)(tile + n * 32 + 4 * (kq ^ (m >> 2)));
;     const unsigned a0 = (m & 1) ? g.y : g.x, a1 = (m & 1) ? g.x : g.y, a2 = (m & 1) ? g.w : g.z, a3 = (m & 1) ? g.z : g.w;
;     u32x4 w; w.x = (m & 2) ? a2 : a0; w.y = (m & 2) ? a3 : a1; w.z = (m & 2) ? a0 : a2; w.w = (m & 2) ? a1 : a3;
;     __builtin_nontemporal_store(w, (u32x4*)(dst + (size_t)r * ldd + k0 + 16 * kq));
; }
; template <int K_, int N_, int MAP_> __device__ __forceinline__ void tjob_b(const Ctx& C, int bid, int G, const float* src, unsigned char* dstb, int nbatch) {
;     constexpr int kt = K_ / 128, ntile = N_ / 64, per = kt * ntile; const int tot = per * nbatch;
;     TReg R0, R1, R2, R3; int kbuf = 0;
;     ...
;     TB_LOAD(R0, bid); TB_LOAD(R1, bid + G); TB_LOAD(R2, bid + 2 * G); TB_LOAD(R3, bid + 3 * G);
;     for (int t = bid; t < tot; t += 4 * G) { TB_STEP(R0, t); TB_STEP(R1, t + G); TB_STEP(R2, t + 2 * G); TB_STEP(R3, t + 3 * G); }
.LBB0_181:
	s_add_i32 s23, s22, s0
	s_cmpk_gt_i32 s23, 0x7fff
	s_cbranch_scc1 .LBB0_183
	s_ashr_i32 s8, s23, 31
	s_lshr_b32 s8, s8, 22
	s_add_i32 s9, s23, s8
	s_ashr_i32 s8, s9, 10
	s_and_b32 s9, s9, 0xfc00
	s_sub_i32 s12, s23, s9
	s_sext_i32_i16 s13, s12
	s_bfe_u32 s13, s13, 0x4001b
	s_add_i32 s13, s12, s13
	s_sext_i32_i16 s14, s13
	s_and_b32 s13, s13, 0xfff0
	s_sub_i32 s12, s12, s13
	s_ashr_i32 s9, s8, 31
	s_sext_i32_i16 s15, s12
	s_lshl_b32 s12, s14, 2
	s_lshl_b64 s[8:9], s[8:9], 25
	s_andn2_b32 s12, s12, 63
	v_and_b32_e32 v1, -4, v69
	s_ashr_i32 s13, s12, 31
	s_waitcnt vmcnt(0) lgkmcnt(0)
	v_lshl_add_u64 v[34:35], v[66:67], 0, s[8:9]
	v_lshl_add_u32 v42, s15, 7, v1
	v_lshl_add_u64 v[34:35], s[12:13], 2, v[34:35]
	v_and_b32_e32 v36, 0xf0, v74
	v_mov_b32_e32 v37, 0
	v_ashrrev_i32_e32 v43, 31, v42
	v_lshl_add_u64 v[44:45], v[34:35], 0, v[36:37]
	v_lshlrev_b64 v[34:35], 14, v[42:43]
	v_lshl_add_u64 v[46:47], v[44:45], 0, v[34:35]
	v_or_b32_e32 v34, 1, v42
	v_ashrrev_i32_e32 v35, 31, v34
	v_lshlrev_b64 v[34:35], 14, v[34:35]
	v_lshl_add_u64 v[48:49], v[44:45], 0, v[34:35]
	global_load_dwordx4 v[34:37], v[46:47], off nt
	global_load_dwordx4 v[38:41], v[48:49], off nt
	v_or_b32_e32 v46, 2, v42
	v_ashrrev_i32_e32 v47, 31, v46
	v_or_b32_e32 v42, 3, v42
	v_lshlrev_b64 v[46:47], 14, v[46:47]
	v_ashrrev_i32_e32 v43, 31, v42
	v_lshl_add_u64 v[50:51], v[44:45], 0, v[46:47]
	v_lshlrev_b64 v[42:43], 14, v[42:43]
	v_lshl_add_u64 v[52:53], v[44:45], 0, v[42:43]
	global_load_dwordx4 v[42:45], v[50:51], off nt
	global_load_dwordx4 v[46:49], v[52:53], off nt
.LBB0_183:
	s_add_i32 s24, s23, s0
	s_cmpk_gt_i32 s24, 0x7fff
	s_cbranch_scc1 .LBB0_185
	s_ashr_i32 s8, s24, 31
	s_lshr_b32 s8, s8, 22
	s_add_i32 s9, s24, s8
	s_ashr_i32 s8, s9, 10
	s_and_b32 s9, s9, 0xfc00
	s_sub_i32 s12, s24, s9
	s_sext_i32_i16 s13, s12
	s_bfe_u32 s13, s13, 0x4001b
	s_add_i32 s13, s12, s13
	s_sext_i32_i16 s14, s13
	s_and_b32 s13, s13, 0xfff0
	s_sub_i32 s12, s12, s13
	s_ashr_i32 s9, s8, 31
	s_sext_i32_i16 s15, s12
	s_lshl_b32 s12, s14, 2
	s_lshl_b64 s[8:9], s[8:9], 25
	s_andn2_b32 s12, s12, 63
	v_and_b32_e32 v1, -4, v69
	s_ashr_i32 s13, s12, 31
	s_waitcnt vmcnt(0) lgkmcnt(0)
	v_lshl_add_u64 v[50:51], v[66:67], 0, s[8:9]
	v_lshl_add_u32 v58, s15, 7, v1
	v_lshl_add_u64 v[50:51], s[12:13], 2, v[50:51]
	v_and_b32_e32 v52, 0xf0, v74
	v_mov_b32_e32 v53, 0
	v_ashrrev_i32_e32 v59, 31, v58
	v_lshl_add_u64 v[60:61], v[50:51], 0, v[52:53]
	v_lshlrev_b64 v[50:51], 14, v[58:59]
	v_lshl_add_u64 v[62:63], v[60:61], 0, v[50:51]
	v_or_b32_e32 v50, 1, v58
	v_ashrrev_i32_e32 v51, 31, v50
	v_lshlrev_b64 v[50:51], 14, v[50:51]
	v_lshl_add_u64 v[64:65], v[60:61], 0, v[50:51]
	global_load_dwordx4 v[50:53], v[62:63], off nt
	global_load_dwordx4 v[54:57], v[64:65], off nt
	v_or_b32_e32 v62, 2, v58
	v_ashrrev_i32_e32 v63, 31, v62
	v_or_b32_e32 v58, 3, v58
	v_lshlrev_b64 v[62:63], 14, v[62:63]
	v_ashrrev_i32_e32 v59, 31, v58
	v_lshl_add_u64 v[70:71], v[60:61], 0, v[62:63]
	v_lshlrev_b64 v[58:59], 14, v[58:59]
	v_lshl_add_u64 v[72:73], v[60:61], 0, v[58:59]
	global_load_dwordx4 v[58:61], v[70:71], off nt
	global_load_dwordx4 v[62:65], v[72:73], off nt
.LBB0_185:
	s_lshl_b32 s14, s0, 1
	s_mul_i32 s15, s0, 3
	s_lshl_b32 s16, s0, 2
	s_andn2_b64 vcc, exec, s[6:7]
	v_ashrrev_i32_e32 v78, 4, v68
	v_lshlrev_b32_e32 v79, 2, v68
	v_ashrrev_i32_e32 v1, 3, v68
	v_and_b32_e32 v75, 7, v68
	v_and_b32_e32 v76, 8, v68
	v_and_b32_e32 v77, 16, v68
	s_mul_i32 s17, s0, 7
	s_mul_i32 s18, s0, 6
	s_mul_i32 s19, s0, 5
	s_cbranch_vccnz .LBB0_202
	v_and_b32_e32 v68, 60, v79
	v_or_b32_e32 v70, 1, v68
	v_bitop3_b32 v89, v70, v78, 29 bitop3:0x6c
	v_lshlrev_b32_e32 v81, 7, v70
	v_or_b32_e32 v70, 2, v68
	v_bitop3_b32 v90, v70, v78, 30 bitop3:0x6c
	v_lshlrev_b32_e32 v82, 7, v70
	v_or_b32_e32 v70, 3, v68
	v_bitop3_b32 v91, v70, v78, 31 bitop3:0x6c
	v_lshlrev_b32_e32 v83, 7, v70
	v_lshlrev_b32_e32 v70, 2, v75
	s_add_u32 s25, s62, 0x9910000
	v_bitop3_b32 v72, v79, v78, 28 bitop3:0x6c
	v_lshlrev_b32_e32 v84, 7, v1
	v_bitop3_b32 v92, v1, v70, 28 bitop3:0x6c
	v_mov_b32_e32 v73, 0
	s_addc_u32 s26, s63, 0
	v_lshlrev_b32_e32 v80, 7, v68
	v_and_b32_e32 v85, 0x80, v84
	s_mov_b32 s27, 0
	v_cmp_eq_u32_e64 s[6:7], 0, v76
	v_cmp_eq_u32_e64 s[8:9], 0, v77
	v_lshlrev_b32_e32 v70, 4, v75
	v_mov_b32_e32 v71, v73
	v_and_b32_e32 v86, -4, v69
	s_mov_b32 s31, 0xc3e00000
	v_mov_b32_e32 v87, 0x43e00000
	v_lshlrev_b32_e32 v88, 2, v72
	v_lshlrev_b32_e32 v89, 2, v89
	v_lshlrev_b32_e32 v90, 2, v90
	v_lshlrev_b32_e32 v91, 2, v91
	v_lshlrev_b32_e32 v92, 2, v92
	s_mov_b32 s34, s1
	s_waitcnt vmcnt(0)
	s_branch .LBB0_189

; #define LAS __attribute__((address_space(3)))
; #define TB_LOAD(R_, t_) do { const int _t = (t_); if (_t < tot) { const int _b = _t / per, _r = _t % per; ttb_load(R_, src + (size_t)_b * K_ * N_, N_, (_r % kt) * 128, (_r / kt) * 64, C.tid); } } while (0)
; #define TB_STEP(R_, t_) do { const int _u = (t_); if (_u < tot) { LAS unsigned* tile = (LAS unsigned*)(C.lds + kbuf * 8192); ttb_put(R_, tile, C.tid); TB_LOAD(R_, _u + 4 * G); __syncthreads(); \
;         { const int _b = _u / per, _r = _u % per; ttb_finish(tile, dstb + (size_t)_b * K_ * (MAP_ == 2 ? 4096 : N_), K_, (_r % kt) * 128, (_r / kt) * 64, MAP_, C.tid); } kbuf ^= 1; } } while (0)
; __device__ __forceinline__ void ttb_put(const TReg& R, LAS unsigned* tile, int tid) {
;     const int kr = tid >> 4, nq = tid & 15;
; #pragma unroll
;     for (int c = 0; c < 4; ++c) { const int n = 4 * nq + c;
;         tile[n * 32 + (kr ^ (n & 31))] = pk4_fp8(R.v[0][c] * W_FP8_SCALE, R.v[1][c] * W_FP8_SCALE, R.v[2][c] * W_FP8_SCALE, R.v[3][c] * W_FP8_SCALE); } }
; __device__ __forceinline__ void ttb_finish(LAS const unsigned* tile, unsigned char* dst, int ldd, int k0, int n0, int map, int tid) {
;     const int n = tid >> 3, kq = tid & 7, m = n & 31, ns = n0 + n; int r = ns;
;     if (map == 2) { const int j = ns >> 1, par = ns & 1; r = 256 * (j >> 7) + 128 * par + (j & 127); }
;     const u32x4 g = *(LAS const u32x4*)(tile + n * 32 + 4 * (kq ^ (m >> 2)));
;     const unsigned a0 = (m & 1) ? g.y : g.x, a1 = (m & 1) ? g.x : g.y, a2 = (m & 1) ? g.w : g.z, a3 = (m & 1) ? g.z : g.w;
;     u32x4 w; w.x = (m & 2) ? a2 : a0; w.y = (m & 2) ? a3 : a1; w.z = (m & 2) ? a0 : a2; w.w = (m & 2) ? a1 : a3;
;     __builtin_nontemporal_store(w, (u32x4*)(dst + (size_t)r * ldd + k0 + 16 * kq));
; }
; template <int K_, int N_, int MAP_> __device__ __forceinline__ void tjob_b(const Ctx& C, int bid, int G, const float* src, unsigned char* dstb, int nbatch) {
;     constexpr int kt = K_ / 128, ntile = N_ / 64, per = kt * ntile; const int tot = per * nbatch;
;     TReg R0, R1, R2, R3; int kbuf = 0;
;     ...
;     TB_LOAD(R0, bid); TB_LOAD(R1, bid + G); TB_LOAD(R2, bid + 2 * G); TB_LOAD(R3, bid + 3 * G);
;     for (int t = bid; t < tot; t += 4 * G) { TB_STEP(R0, t); TB_STEP(R1, t + G); TB_STEP(R2, t + 2 * G); TB_STEP(R3, t + 3 * G); }
.LBB0_189:
	s_waitcnt vmcnt(16) lgkmcnt(0)
	s_add_i32 s36, s34, s15
	s_cmp_lt_i32 s36, 0x8000
	s_cbranch_scc1 .Lcv_j1_0
	s_waitcnt vmcnt(0)
.Lcv_j1_0:
	v_mul_f32_e32 v72, 0x43800000, v2
	v_mul_f32_e32 v93, 0x43800000, v6
	v_med3_f32 v72, v72, s31, v87
	v_med3_f32 v93, v93, s31, v87
	v_cvt_pk_fp8_f32 v95, v72, v93
	v_mul_f32_e32 v94, 0x43800000, v10
	v_mul_f32_e32 v72, 0x43800000, v14
	v_med3_f32 v93, v94, s31, v87
	v_med3_f32 v72, v72, s31, v87
	v_cvt_pk_fp8_f32 v95, v93, v72 op_sel:[0,0,1]
	v_mul_f32_e32 v72, 0x43800000, v3
	v_mul_f32_e32 v93, 0x43800000, v7
	v_med3_f32 v72, v72, s31, v87
	v_med3_f32 v93, v93, s31, v87
	v_cvt_pk_fp8_f32 v96, v72, v93
	v_mul_f32_e32 v94, 0x43800000, v11
	v_mul_f32_e32 v72, 0x43800000, v15
	v_med3_f32 v93, v94, s31, v87
	v_med3_f32 v72, v72, s31, v87
	s_lshl_b32 s12, s27, 13
	v_cvt_pk_fp8_f32 v96, v93, v72 op_sel:[0,0,1]
	s_add_i32 s35, s12, 0
	v_add3_u32 v72, s35, v80, v88
	ds_write_b32 v72, v95
	v_add3_u32 v72, s35, v81, v89
	ds_write_b32 v72, v96
	v_mul_f32_e32 v72, 0x43800000, v4
	v_mul_f32_e32 v93, 0x43800000, v8
	v_med3_f32 v72, v72, s31, v87
	v_med3_f32 v93, v93, s31, v87
	v_cvt_pk_fp8_f32 v95, v72, v93
	v_mul_f32_e32 v94, 0x43800000, v12
	v_mul_f32_e32 v72, 0x43800000, v16
	v_med3_f32 v93, v94, s31, v87
	v_med3_f32 v72, v72, s31, v87
	v_cvt_pk_fp8_f32 v95, v93, v72 op_sel:[0,0,1]
	v_mul_f32_e32 v72, 0x43800000, v5
	v_mul_f32_e32 v93, 0x43800000, v9
	v_med3_f32 v72, v72, s31, v87
	v_med3_f32 v93, v93, s31, v87
	v_cvt_pk_fp8_f32 v96, v72, v93
	v_mul_f32_e32 v94, 0x43800000, v13
	v_mul_f32_e32 v72, 0x43800000, v17
	v_med3_f32 v93, v94, s31, v87
	v_med3_f32 v72, v72, s31, v87
	v_cvt_pk_fp8_f32 v96, v93, v72 op_sel:[0,0,1]
	s_add_i32 s33, s34, s16
	s_cmpk_gt_i32 s33, 0x7fff
	v_add3_u32 v72, s35, v82, v90
	s_cselect_b64 s[12:13], -1, 0
	ds_write_b32 v72, v95
	v_add3_u32 v72, s35, v83, v91
	s_and_b64 vcc, exec, s[12:13]
	ds_write_b32 v72, v96
	s_cbranch_vccnz .LBB0_191
	s_ashr_i32 s36, s33, 31
	s_lshr_b32 s36, s36, 22
	s_add_i32 s37, s33, s36
	s_ashr_i32 s36, s37, 10
	s_and_b32 s37, s37, 0xfc00
	s_sub_i32 s38, s33, s37
	s_ashr_i32 s37, s36, 31
	s_lshl_b64 s[36:37], s[36:37], 25
	v_lshl_add_u64 v[2:3], v[66:67], 0, s[36:37]
	s_sext_i32_i16 s36, s38
	s_bfe_u32 s36, s36, 0x4001b
	s_add_i32 s36, s38, s36
	s_sext_i32_i16 s37, s36
	s_and_b32 s36, s36, 0xfff0
	s_sub_i32 s36, s38, s36
	s_sext_i32_i16 s38, s36
	s_lshl_b32 s36, s37, 2
	s_andn2_b32 s36, s36, 63
	v_lshl_add_u32 v10, s38, 7, v86
	s_ashr_i32 s37, s36, 31
	v_lshl_add_u64 v[2:3], s[36:37], 2, v[2:3]
	v_lshlrev_b32_e32 v72, 2, v68
	v_ashrrev_i32_e32 v11, 31, v10
	v_lshl_add_u64 v[12:13], v[2:3], 0, v[72:73]
	v_lshlrev_b64 v[2:3], 14, v[10:11]
	v_or_b32_e32 v4, 1, v10
	v_or_b32_e32 v14, 2, v10
	v_or_b32_e32 v10, 3, v10
	v_ashrrev_i32_e32 v5, 31, v4
	v_ashrrev_i32_e32 v15, 31, v14
	v_ashrrev_i32_e32 v11, 31, v10
	v_lshlrev_b64 v[4:5], 14, v[4:5]
	v_lshlrev_b64 v[14:15], 14, v[14:15]
	v_lshlrev_b64 v[10:11], 14, v[10:11]
	v_lshl_add_u64 v[2:3], v[12:13], 0, v[2:3]
	v_lshl_add_u64 v[6:7], v[12:13], 0, v[4:5]
	v_lshl_add_u64 v[14:15], v[12:13], 0, v[14:15]
	v_lshl_add_u64 v[16:17], v[12:13], 0, v[10:11]
	global_load_dwordx4 v[2:5], v[2:3], off nt
	s_nop 0
	global_load_dwordx4 v[6:9], v[6:7], off nt
	s_nop 0
	global_load_dwordx4 v[10:13], v[14:15], off nt
	s_nop 0
	global_load_dwordx4 v[14:17], v[16:17], off nt
; #define LAS __attribute__((address_space(3)))
; #define TB_LOAD(R_, t_) do { const int _t = (t_); if (_t < tot) { const int _b = _t / per, _r = _t % per; ttb_load(R_, src + (size_t)_b * K_ * N_, N_, (_r % kt) * 128, (_r / kt) * 64, C.tid); } } while (0)
; #define TB_STEP(R_, t_) do { const int _u = (t_); if (_u < tot) { LAS unsigned* tile = (LAS unsigned*)(C.lds + kbuf * 8192); ttb_put(R_, tile, C.tid); TB_LOAD(R_, _u + 4 * G); __syncthreads(); \
;         { const int _b = _u / per, _r = _u % per; ttb_finish(tile, dstb + (size_t)_b * K_ * (MAP_ == 2 ? 4096 : N_), K_, (_r % kt) * 128, (_r / kt) * 64, MAP_, C.tid); } kbuf ^= 1; } } while (0)
; __device__ __forceinline__ void ttb_put(const TReg& R, LAS unsigned* tile, int tid) {
;     const int kr = tid >> 4, nq = tid & 15;
; #pragma unroll
;     for (int c = 0; c < 4; ++c) { const int n = 4 * nq + c;
;         tile[n * 32 + (kr ^ (n & 31))] = pk4_fp8(R.v[0][c] * W_FP8_SCALE, R.v[1][c] * W_FP8_SCALE, R.v[2][c] * W_FP8_SCALE, R.v[3][c] * W_FP8_SCALE); } }
; __device__ __forceinline__ void ttb_finish(LAS const unsigned* tile, unsigned char* dst, int ldd, int k0, int n0, int map, int tid) {
;     const int n = tid >> 3, kq = tid & 7, m = n & 31, ns = n0 + n; int r = ns;
;     if (map == 2) { const int j = ns >> 1, par = ns & 1; r = 256 * (j >> 7) + 128 * par + (j & 127); }
;     const u32x4 g = *(LAS const u32x4*)(tile + n * 32 + 4 * (kq ^ (m >> 2)));
;     const unsigned a0 = (m & 1) ? g.y : g.x, a1 = (m & 1) ? g.x : g.y, a2 = (m & 1) ? g.w : g.z, a3 = (m & 1) ? g.z : g.w;
;     u32x4 w; w.x = (m & 2) ? a2 : a0; w.y = (m & 2) ? a3 : a1; w.z = (m & 2) ? a0 : a2; w.w = (m & 2) ? a1 : a3;
;     __builtin_nontemporal_store(w, (u32x4*)(dst + (size_t)r * ldd + k0 + 16 * kq));
; }
; template <int K_, int N_, int MAP_> __device__ __forceinline__ void tjob_b(const Ctx& C, int bid, int G, const float* src, unsigned char* dstb, int nbatch) {
;     constexpr int kt = K_ / 128, ntile = N_ / 64, per = kt * ntile; const int tot = per * nbatch;
;     TReg R0, R1, R2, R3; int kbuf = 0;
;     ...
;     TB_LOAD(R0, bid); TB_LOAD(R1, bid + G); TB_LOAD(R2, bid + 2 * G); TB_LOAD(R3, bid + 3 * G);
;     for (int t = bid; t < tot; t += 4 * G) { TB_STEP(R0, t); TB_STEP(R1, t + G); TB_STEP(R2, t + 2 * G); TB_STEP(R3, t + 3 * G); }
.LBB0_191:
	s_ashr_i32 s36, s34, 31
	s_lshr_b32 s36, s36, 22
	s_add_i32 s37, s34, s36
	s_ashr_i32 s36, s37, 10
	s_and_b32 s37, s37, 0xfc00
	s_sub_i32 s38, s34, s37
	s_ashr_i32 s37, s36, 31
	s_lshl_b64 s[36:37], s[36:37], 23
	s_add_u32 s36, s25, s36
	s_sext_i32_i16 s39, s38
	s_addc_u32 s37, s26, s37
	s_bfe_u32 s39, s39, 0x4001b
	s_add_i32 s39, s38, s39
	v_add3_u32 v72, s35, v84, v92
	s_waitcnt lgkmcnt(0)
	s_barrier
	s_sext_i32_i16 s40, s39
	s_and_b32 s39, s39, 0xfff0
	ds_read_b128 v[94:97], v72
	s_sub_i32 s38, s38, s39
	s_lshl_b32 s39, s40, 2
	s_andn2_b32 s39, s39, 63
	v_add_u32_e32 v72, s39, v1
	v_and_b32_e32 v93, 0xffffff00, v72
	v_bfe_u32 v72, v72, 1, 7
	v_or3_b32 v98, v93, v72, v85
	s_waitcnt lgkmcnt(0)
	v_cndmask_b32_e64 v72, v95, v94, s[6:7]
	v_cndmask_b32_e64 v99, v97, v96, s[6:7]
	s_sext_i32_i16 s38, s38
	v_cndmask_b32_e64 v93, v94, v95, s[6:7]
	v_cndmask_b32_e64 v97, v96, v97, s[6:7]
	v_cndmask_b32_e64 v94, v99, v72, s[8:9]
	v_cndmask_b32_e64 v96, v72, v99, s[8:9]
	v_ashrrev_i32_e32 v99, 31, v98
	s_lshl_b32 s38, s38, 7
	v_lshlrev_b64 v[98:99], 11, v[98:99]
	v_lshl_add_u64 v[98:99], s[36:37], 0, v[98:99]
	s_ashr_i32 s39, s38, 31
	v_lshl_add_u64 v[98:99], v[98:99], 0, s[38:39]
	s_xor_b32 s36, s27, 1
	s_add_i32 s35, s0, s34
	v_cndmask_b32_e64 v95, v97, v93, s[8:9]
	v_cndmask_b32_e64 v97, v93, v97, s[8:9]
	v_lshl_add_u64 v[98:99], v[98:99], 0, v[70:71]
	s_cmpk_gt_i32 s35, 0x7fff
	global_store_dwordx4 v[98:99], v[94:97], off nt
	s_cbranch_scc1 .LBB0_195
	s_waitcnt vmcnt(16)
	s_add_i32 s37, s35, s15
	s_cmp_lt_i32 s37, 0x8000
	s_cbranch_scc1 .Lcv_j1_1
	s_waitcnt vmcnt(0)
.Lcv_j1_1:
	v_mul_f32_e32 v72, 0x43800000, v18
	v_mul_f32_e32 v93, 0x43800000, v22
	v_med3_f32 v72, v72, s31, v87
	v_med3_f32 v93, v93, s31, v87
	v_cvt_pk_fp8_f32 v95, v72, v93
	v_mul_f32_e32 v94, 0x43800000, v26
	v_mul_f32_e32 v72, 0x43800000, v30
	v_med3_f32 v93, v94, s31, v87
	v_med3_f32 v72, v72, s31, v87
	v_cvt_pk_fp8_f32 v95, v93, v72 op_sel:[0,0,1]
	s_lshl_b32 s36, s36, 13
	s_add_i32 s36, s36, 0
	v_add3_u32 v72, s36, v80, v88
	ds_write_b32 v72, v95
	v_mul_f32_e32 v72, 0x43800000, v19
	v_mul_f32_e32 v93, 0x43800000, v23
	v_med3_f32 v72, v72, s31, v87
	v_med3_f32 v93, v93, s31, v87
	v_cvt_pk_fp8_f32 v95, v72, v93
	v_mul_f32_e32 v94, 0x43800000, v27
	v_mul_f32_e32 v72, 0x43800000, v31
	v_med3_f32 v93, v94, s31, v87
	v_med3_f32 v72, v72, s31, v87
	v_cvt_pk_fp8_f32 v95, v93, v72 op_sel:[0,0,1]
	v_mul_f32_e32 v72, 0x43800000, v20
	v_mul_f32_e32 v93, 0x43800000, v24
	v_med3_f32 v72, v72, s31, v87
	v_med3_f32 v93, v93, s31, v87
	v_cvt_pk_fp8_f32 v96, v72, v93
	v_mul_f32_e32 v94, 0x43800000, v28
	v_mul_f32_e32 v72, 0x43800000, v32
	v_med3_f32 v93, v94, s31, v87
	v_med3_f32 v72, v72, s31, v87
	v_cvt_pk_fp8_f32 v96, v93, v72 op_sel:[0,0,1]
	v_add3_u32 v72, s36, v81, v89
	ds_write_b32 v72, v95
	v_add3_u32 v72, s36, v82, v90
	ds_write_b32 v72, v96
	v_mul_f32_e32 v72, 0x43800000, v21
	v_mul_f32_e32 v93, 0x43800000, v25
	v_med3_f32 v72, v72, s31, v87
	v_med3_f32 v93, v93, s31, v87
	v_cvt_pk_fp8_f32 v95, v72, v93
	v_mul_f32_e32 v94, 0x43800000, v29
	v_mul_f32_e32 v72, 0x43800000, v33
	v_med3_f32 v93, v94, s31, v87
	v_med3_f32 v72, v72, s31, v87
	v_cvt_pk_fp8_f32 v95, v93, v72 op_sel:[0,0,1]
	s_add_i32 s37, s19, s34
	v_add3_u32 v72, s36, v83, v91
	s_cmpk_gt_i32 s37, 0x7fff
	ds_write_b32 v72, v95
	s_cbranch_scc1 .LBB0_194
	s_ashr_i32 s38, s37, 31
	s_lshr_b32 s38, s38, 22
	s_add_i32 s39, s37, s38
	s_ashr_i32 s38, s39, 10
	s_and_b32 s39, s39, 0xfc00
	s_sub_i32 s37, s37, s39
	s_ashr_i32 s39, s38, 31
	s_lshl_b64 s[38:39], s[38:39], 25
	v_lshl_add_u64 v[18:19], v[66:67], 0, s[38:39]
	s_sext_i32_i16 s38, s37
	s_bfe_u32 s38, s38, 0x4001b
	s_add_i32 s38, s37, s38
	s_sext_i32_i16 s39, s38
	s_and_b32 s38, s38, 0xfff0
	s_sub_i32 s37, s37, s38
	s_lshl_b32 s38, s39, 2
	s_sext_i32_i16 s37, s37
	s_andn2_b32 s38, s38, 63
	v_lshl_add_u32 v26, s37, 7, v86
	s_ashr_i32 s39, s38, 31
	v_lshl_add_u64 v[18:19], s[38:39], 2, v[18:19]
	v_lshlrev_b32_e32 v72, 2, v68
	v_ashrrev_i32_e32 v27, 31, v26
	v_lshl_add_u64 v[28:29], v[18:19], 0, v[72:73]
	v_lshlrev_b64 v[18:19], 14, v[26:27]
	v_or_b32_e32 v20, 1, v26
	v_or_b32_e32 v30, 2, v26
	v_or_b32_e32 v26, 3, v26
	v_ashrrev_i32_e32 v21, 31, v20
	v_ashrrev_i32_e32 v31, 31, v30
	v_ashrrev_i32_e32 v27, 31, v26
	v_lshlrev_b64 v[20:21], 14, v[20:21]
	v_lshlrev_b64 v[30:31], 14, v[30:31]
	v_lshlrev_b64 v[26:27], 14, v[26:27]
	v_lshl_add_u64 v[18:19], v[28:29], 0, v[18:19]
	v_lshl_add_u64 v[22:23], v[28:29], 0, v[20:21]
	v_lshl_add_u64 v[30:31], v[28:29], 0, v[30:31]
	v_lshl_add_u64 v[32:33], v[28:29], 0, v[26:27]
	global_load_dwordx4 v[18:21], v[18:19], off nt
	s_nop 0
	global_load_dwordx4 v[22:25], v[22:23], off nt
	s_nop 0
	global_load_dwordx4 v[26:29], v[30:31], off nt
	s_nop 0
	global_load_dwordx4 v[30:33], v[32:33], off nt

; #define LAS __attribute__((address_space(3)))
; #define TB_LOAD(R_, t_) do { const int _t = (t_); if (_t < tot) { const int _b = _t / per, _r = _t % per; ttb_load(R_, src + (size_t)_b * K_ * N_, N_, (_r % kt) * 128, (_r / kt) * 64, C.tid); } } while (0)
; #define TB_STEP(R_, t_) do { const int _u = (t_); if (_u < tot) { LAS unsigned* tile = (LAS unsigned*)(C.lds + kbuf * 8192); ttb_put(R_, tile, C.tid); TB_LOAD(R_, _u + 4 * G); __syncthreads(); \
;         { const int _b = _u / per, _r = _u % per; ttb_finish(tile, dstb + (size_t)_b * K_ * (MAP_ == 2 ? 4096 : N_), K_, (_r % kt) * 128, (_r / kt) * 64, MAP_, C.tid); } kbuf ^= 1; } } while (0)
; __device__ __forceinline__ void ttb_put(const TReg& R, LAS unsigned* tile, int tid) {
;     const int kr = tid >> 4, nq = tid & 15;
; #pragma unroll
;     for (int c = 0; c < 4; ++c) { const int n = 4 * nq + c;
;         tile[n * 32 + (kr ^ (n & 31))] = pk4_fp8(R.v[0][c] * W_FP8_SCALE, R.v[1][c] * W_FP8_SCALE, R.v[2][c] * W_FP8_SCALE, R.v[3][c] * W_FP8_SCALE); } }
; __device__ __forceinline__ void ttb_finish(LAS const unsigned* tile, unsigned char* dst, int ldd, int k0, int n0, int map, int tid) {
;     const int n = tid >> 3, kq = tid & 7, m = n & 31, ns = n0 + n; int r = ns;
;     if (map == 2) { const int j = ns >> 1, par = ns & 1; r = 256 * (j >> 7) + 128 * par + (j & 127); }
;     const u32x4 g = *(LAS const u32x4*)(tile + n * 32 + 4 * (kq ^ (m >> 2)));
;     const unsigned a0 = (m & 1) ? g.y : g.x, a1 = (m & 1) ? g.x : g.y, a2 = (m & 1) ? g.w : g.z, a3 = (m & 1) ? g.z : g.w;
;     u32x4 w; w.x = (m & 2) ? a2 : a0; w.y = (m & 2) ? a3 : a1; w.z = (m & 2) ? a0 : a2; w.w = (m & 2) ? a1 : a3;
;     __builtin_nontemporal_store(w, (u32x4*)(dst + (size_t)r * ldd + k0 + 16 * kq));
; }
; template <int K_, int N_, int MAP_> __device__ __forceinline__ void tjob_b(const Ctx& C, int bid, int G, const float* src, unsigned char* dstb, int nbatch) {
;     constexpr int kt = K_ / 128, ntile = N_ / 64, per = kt * ntile; const int tot = per * nbatch;
;     TReg R0, R1, R2, R3; int kbuf = 0;
;     ...
;     TB_LOAD(R0, bid); TB_LOAD(R1, bid + G); TB_LOAD(R2, bid + 2 * G); TB_LOAD(R3, bid + 3 * G);
;     for (int t = bid; t < tot; t += 4 * G) { TB_STEP(R0, t); TB_STEP(R1, t + G); TB_STEP(R2, t + 2 * G); TB_STEP(R3, t + 3 * G); }
.LBB0_196:
	s_waitcnt vmcnt(16)
	s_add_i32 s37, s36, s15
	s_cmp_lt_i32 s37, 0x8000
	s_cbranch_scc1 .Lcv_j1_2
	s_waitcnt vmcnt(0)
.Lcv_j1_2:
	v_mul_f32_e32 v72, 0x43800000, v34
	v_mul_f32_e32 v93, 0x43800000, v38
	v_med3_f32 v72, v72, s31, v87
	v_med3_f32 v93, v93, s31, v87
	v_cvt_pk_fp8_f32 v95, v72, v93
	v_mul_f32_e32 v94, 0x43800000, v42
	v_mul_f32_e32 v72, 0x43800000, v46
	v_med3_f32 v93, v94, s31, v87
	v_med3_f32 v72, v72, s31, v87
	v_cvt_pk_fp8_f32 v95, v93, v72 op_sel:[0,0,1]
	s_lshl_b32 s35, s27, 13
	s_add_i32 s35, s35, 0
	v_add3_u32 v72, s35, v80, v88
	ds_write_b32 v72, v95
	v_mul_f32_e32 v72, 0x43800000, v35
	v_mul_f32_e32 v93, 0x43800000, v39
	v_med3_f32 v72, v72, s31, v87
	v_med3_f32 v93, v93, s31, v87
	v_cvt_pk_fp8_f32 v95, v72, v93
	v_mul_f32_e32 v94, 0x43800000, v43
	v_mul_f32_e32 v72, 0x43800000, v47
	v_med3_f32 v93, v94, s31, v87
	v_med3_f32 v72, v72, s31, v87
	v_cvt_pk_fp8_f32 v95, v93, v72 op_sel:[0,0,1]
	v_mul_f32_e32 v72, 0x43800000, v36
	v_mul_f32_e32 v93, 0x43800000, v40
	v_med3_f32 v72, v72, s31, v87
	v_med3_f32 v93, v93, s31, v87
	v_cvt_pk_fp8_f32 v96, v72, v93
	v_mul_f32_e32 v94, 0x43800000, v44
	v_mul_f32_e32 v72, 0x43800000, v48
	v_med3_f32 v93, v94, s31, v87
	v_med3_f32 v72, v72, s31, v87
	v_cvt_pk_fp8_f32 v96, v93, v72 op_sel:[0,0,1]
	v_add3_u32 v72, s35, v81, v89
	ds_write_b32 v72, v95
	v_add3_u32 v72, s35, v82, v90
	ds_write_b32 v72, v96
	v_mul_f32_e32 v72, 0x43800000, v37
	v_mul_f32_e32 v93, 0x43800000, v41
	v_med3_f32 v72, v72, s31, v87
	v_med3_f32 v93, v93, s31, v87
	v_cvt_pk_fp8_f32 v95, v72, v93
	v_mul_f32_e32 v94, 0x43800000, v45
	v_mul_f32_e32 v72, 0x43800000, v49
	v_med3_f32 v93, v94, s31, v87
	v_med3_f32 v72, v72, s31, v87
	v_cvt_pk_fp8_f32 v95, v93, v72 op_sel:[0,0,1]
	s_add_i32 s37, s18, s34
	v_add3_u32 v72, s35, v83, v91
	s_cmpk_gt_i32 s37, 0x7fff
	ds_write_b32 v72, v95
	s_cbranch_scc1 .LBB0_198
	s_ashr_i32 s38, s37, 31
	s_lshr_b32 s38, s38, 22
	s_add_i32 s39, s37, s38
	s_ashr_i32 s38, s39, 10
	s_and_b32 s39, s39, 0xfc00
	s_sub_i32 s37, s37, s39
	s_ashr_i32 s39, s38, 31
	s_lshl_b64 s[38:39], s[38:39], 25
	v_lshl_add_u64 v[34:35], v[66:67], 0, s[38:39]
	s_sext_i32_i16 s38, s37
	s_bfe_u32 s38, s38, 0x4001b
	s_add_i32 s38, s37, s38
	s_sext_i32_i16 s39, s38
	s_and_b32 s38, s38, 0xfff0
	s_sub_i32 s37, s37, s38
	s_lshl_b32 s38, s39, 2
	s_sext_i32_i16 s37, s37
	s_andn2_b32 s38, s38, 63
	v_lshl_add_u32 v42, s37, 7, v86
	s_ashr_i32 s39, s38, 31
	v_lshl_add_u64 v[34:35], s[38:39], 2, v[34:35]
	v_lshlrev_b32_e32 v72, 2, v68
	v_ashrrev_i32_e32 v43, 31, v42
	v_lshl_add_u64 v[44:45], v[34:35], 0, v[72:73]
	v_lshlrev_b64 v[34:35], 14, v[42:43]
	v_or_b32_e32 v36, 1, v42
	v_or_b32_e32 v46, 2, v42
	v_or_b32_e32 v42, 3, v42
	v_ashrrev_i32_e32 v37, 31, v36
	v_ashrrev_i32_e32 v47, 31, v46
	v_ashrrev_i32_e32 v43, 31, v42
	v_lshlrev_b64 v[36:37], 14, v[36:37]
	v_lshlrev_b64 v[46:47], 14, v[46:47]
	v_lshlrev_b64 v[42:43], 14, v[42:43]
	v_lshl_add_u64 v[34:35], v[44:45], 0, v[34:35]
	v_lshl_add_u64 v[38:39], v[44:45], 0, v[36:37]
	v_lshl_add_u64 v[46:47], v[44:45], 0, v[46:47]
	v_lshl_add_u64 v[48:49], v[44:45], 0, v[42:43]
	global_load_dwordx4 v[34:37], v[34:35], off nt
	s_nop 0
	global_load_dwordx4 v[38:41], v[38:39], off nt
	s_nop 0
	global_load_dwordx4 v[42:45], v[46:47], off nt
	s_nop 0
	global_load_dwordx4 v[46:49], v[48:49], off nt

; #define LAS __attribute__((address_space(3)))
; #define TB_LOAD(R_, t_) do { const int _t = (t_); if (_t < tot) { const int _b = _t / per, _r = _t % per; ttb_load(R_, src + (size_t)_b * K_ * N_, N_, (_r % kt) * 128, (_r / kt) * 64, C.tid); } } while (0)
; #define TB_STEP(R_, t_) do { const int _u = (t_); if (_u < tot) { LAS unsigned* tile = (LAS unsigned*)(C.lds + kbuf * 8192); ttb_put(R_, tile, C.tid); TB_LOAD(R_, _u + 4 * G); __syncthreads(); \
;         { const int _b = _u / per, _r = _u % per; ttb_finish(tile, dstb + (size_t)_b * K_ * (MAP_ == 2 ? 4096 : N_), K_, (_r % kt) * 128, (_r / kt) * 64, MAP_, C.tid); } kbuf ^= 1; } } while (0)
; __device__ __forceinline__ void ttb_put(const TReg& R, LAS unsigned* tile, int tid) {
;     const int kr = tid >> 4, nq = tid & 15;
; #pragma unroll
;     for (int c = 0; c < 4; ++c) { const int n = 4 * nq + c;
;         tile[n * 32 + (kr ^ (n & 31))] = pk4_fp8(R.v[0][c] * W_FP8_SCALE, R.v[1][c] * W_FP8_SCALE, R.v[2][c] * W_FP8_SCALE, R.v[3][c] * W_FP8_SCALE); } }
; __device__ __forceinline__ void ttb_finish(LAS const unsigned* tile, unsigned char* dst, int ldd, int k0, int n0, int map, int tid) {
;     const int n = tid >> 3, kq = tid & 7, m = n & 31, ns = n0 + n; int r = ns;
;     if (map == 2) { const int j = ns >> 1, par = ns & 1; r = 256 * (j >> 7) + 128 * par + (j & 127); }
;     const u32x4 g = *(LAS const u32x4*)(tile + n * 32 + 4 * (kq ^ (m >> 2)));
;     const unsigned a0 = (m & 1) ? g.y : g.x, a1 = (m & 1) ? g.x : g.y, a2 = (m & 1) ? g.w : g.z, a3 = (m & 1) ? g.z : g.w;
;     u32x4 w; w.x = (m & 2) ? a2 : a0; w.y = (m & 2) ? a3 : a1; w.z = (m & 2) ? a0 : a2; w.w = (m & 2) ? a1 : a3;
;     __builtin_nontemporal_store(w, (u32x4*)(dst + (size_t)r * ldd + k0 + 16 * kq));
; }
; template <int K_, int N_, int MAP_> __device__ __forceinline__ void tjob_b(const Ctx& C, int bid, int G, const float* src, unsigned char* dstb, int nbatch) {
;     constexpr int kt = K_ / 128, ntile = N_ / 64, per = kt * ntile; const int tot = per * nbatch;
;     TReg R0, R1, R2, R3; int kbuf = 0;
;     ...
;     TB_LOAD(R0, bid); TB_LOAD(R1, bid + G); TB_LOAD(R2, bid + 2 * G); TB_LOAD(R3, bid + 3 * G);
;     for (int t = bid; t < tot; t += 4 * G) { TB_STEP(R0, t); TB_STEP(R1, t + G); TB_STEP(R2, t + 2 * G); TB_STEP(R3, t + 3 * G); }
.LBB0_199:
	s_add_i32 s36, s15, s34
	s_cmpk_gt_i32 s36, 0x7fff
	s_cbranch_scc1 .LBB0_188
	s_waitcnt vmcnt(16)
	s_add_i32 s37, s36, s15
	s_cmp_lt_i32 s37, 0x8000
	s_cbranch_scc1 .Lcv_j1_3
	s_waitcnt vmcnt(0)
.Lcv_j1_3:
	v_mul_f32_e32 v72, 0x43800000, v50
	v_mul_f32_e32 v93, 0x43800000, v54
	v_med3_f32 v72, v72, s31, v87
	v_med3_f32 v93, v93, s31, v87
	v_cvt_pk_fp8_f32 v95, v72, v93
	v_mul_f32_e32 v94, 0x43800000, v58
	v_mul_f32_e32 v72, 0x43800000, v62
	v_med3_f32 v93, v94, s31, v87
	v_med3_f32 v72, v72, s31, v87
	v_cvt_pk_fp8_f32 v95, v93, v72 op_sel:[0,0,1]
	s_lshl_b32 s35, s27, 13
	s_add_i32 s35, s35, 0
	v_add3_u32 v72, s35, v80, v88
	ds_write_b32 v72, v95
	v_mul_f32_e32 v72, 0x43800000, v51
	v_mul_f32_e32 v93, 0x43800000, v55
	v_med3_f32 v72, v72, s31, v87
	v_med3_f32 v93, v93, s31, v87
	v_cvt_pk_fp8_f32 v95, v72, v93
	v_mul_f32_e32 v94, 0x43800000, v59
	v_mul_f32_e32 v72, 0x43800000, v63
	v_med3_f32 v93, v94, s31, v87
	v_med3_f32 v72, v72, s31, v87
	v_cvt_pk_fp8_f32 v95, v93, v72 op_sel:[0,0,1]
	v_mul_f32_e32 v72, 0x43800000, v52
	v_mul_f32_e32 v93, 0x43800000, v56
	v_med3_f32 v72, v72, s31, v87
	v_med3_f32 v93, v93, s31, v87
	v_cvt_pk_fp8_f32 v96, v72, v93
	v_mul_f32_e32 v94, 0x43800000, v60
	v_mul_f32_e32 v72, 0x43800000, v64
	v_med3_f32 v93, v94, s31, v87
	v_med3_f32 v72, v72, s31, v87
	v_cvt_pk_fp8_f32 v96, v93, v72 op_sel:[0,0,1]
	v_add3_u32 v72, s35, v81, v89
	ds_write_b32 v72, v95
	v_add3_u32 v72, s35, v82, v90
	ds_write_b32 v72, v96
	v_mul_f32_e32 v72, 0x43800000, v53
	v_mul_f32_e32 v93, 0x43800000, v57
	v_med3_f32 v72, v72, s31, v87
	v_med3_f32 v93, v93, s31, v87
	v_cvt_pk_fp8_f32 v95, v72, v93
	v_mul_f32_e32 v94, 0x43800000, v61
	v_mul_f32_e32 v72, 0x43800000, v65
	v_med3_f32 v93, v94, s31, v87
	v_med3_f32 v72, v72, s31, v87
	v_cvt_pk_fp8_f32 v95, v93, v72 op_sel:[0,0,1]
	s_add_i32 s34, s17, s34
	v_add3_u32 v72, s35, v83, v91
	s_cmpk_gt_i32 s34, 0x7fff
	ds_write_b32 v72, v95
	s_cbranch_scc1 .LBB0_187
	s_ashr_i32 s37, s34, 31
	s_lshr_b32 s37, s37, 22
	s_add_i32 s37, s34, s37
	s_ashr_i32 s38, s37, 10
	s_and_b32 s37, s37, 0xfc00
	s_sub_i32 s34, s34, s37
	s_sext_i32_i16 s37, s34
	s_ashr_i32 s39, s38, 31
	s_bfe_u32 s37, s37, 0x4001b
	s_lshl_b64 s[38:39], s[38:39], 25
	s_add_i32 s37, s34, s37
	v_lshl_add_u64 v[50:51], v[66:67], 0, s[38:39]
	s_sext_i32_i16 s38, s37
	s_and_b32 s37, s37, 0xfff0
	s_sub_i32 s34, s34, s37
	s_lshl_b32 s37, s38, 2
	s_sext_i32_i16 s34, s34
	s_and_b32 s38, s37, 0xffffffc0
	v_lshl_add_u32 v58, s34, 7, v86
	s_ashr_i32 s39, s38, 31
	v_lshl_add_u64 v[50:51], s[38:39], 2, v[50:51]
	v_lshlrev_b32_e32 v72, 2, v68
	v_ashrrev_i32_e32 v59, 31, v58
	v_lshl_add_u64 v[60:61], v[50:51], 0, v[72:73]
	v_lshlrev_b64 v[50:51], 14, v[58:59]
	v_or_b32_e32 v52, 1, v58
	v_or_b32_e32 v62, 2, v58
	v_or_b32_e32 v58, 3, v58
	v_ashrrev_i32_e32 v53, 31, v52
	v_ashrrev_i32_e32 v63, 31, v62
	v_ashrrev_i32_e32 v59, 31, v58
	v_lshlrev_b64 v[52:53], 14, v[52:53]
	v_lshlrev_b64 v[62:63], 14, v[62:63]
	v_lshlrev_b64 v[58:59], 14, v[58:59]
	v_lshl_add_u64 v[50:51], v[60:61], 0, v[50:51]
	v_lshl_add_u64 v[54:55], v[60:61], 0, v[52:53]
	v_lshl_add_u64 v[62:63], v[60:61], 0, v[62:63]
	v_lshl_add_u64 v[64:65], v[60:61], 0, v[58:59]
	global_load_dwordx4 v[50:53], v[50:51], off nt
	s_nop 0
	global_load_dwordx4 v[54:57], v[54:55], off nt
	s_nop 0
	global_load_dwordx4 v[58:61], v[62:63], off nt
	s_nop 0
	global_load_dwordx4 v[62:65], v[64:65], off nt
	s_branch .LBB0_187
